# P2c: drop compiler vmcnt(0) behind state-fragment loads, hg_out leaves next gate-tile DMA in flight; P5: next tile's token-id loads no longer waited at tile top (offsets formed in last K step)
# speedup vs baseline: 1.0147x; 1.0147x over previous
; __device__ __forceinline__ float bf2f(bf16_t b) { return __uint_as_float(((unsigned)b) << 16); }
; __device__ __forceinline__ bf16_t f2bf(float v) { return (bf16_t)(cvt_pk_bf16(v, 0.f) & 0xffffu); }
; __device__ __forceinline__ void hg_out_phase(const Params& p, Frame& F) {
;     ...
;           for (int j = 0; j < 16; ++j) { const float bt = off + cs[j]; const int t = 16 * tq + j, sw = t * 128 + ((((k >> 3) ^ (t & 15)) << 3) | (k & 7));
;               QR[sw] = f2bf(rq[j] * __expf(bt)); ZR[sw] = f2bf(kk[j] * __expf(-bt)); } }
;         float gv[4][4];
; #pragma unroll
;         for (int i = 0; i < 4; ++i)
; #pragma unroll
;             for (int nb = 0; nb < 4; ++nb) gv[i][nb] = bf2f(GR[(16 * tb + 4 * fq + i) * 128 + 16 * (4 * vh + nb) + fr]);
.LBB0_577:
	v_add_f32_e32 v68, v68, v197
	v_mul_f32_e32 v199, 0x3fb8aa3b, v68
	v_exp_f32_e32 v199, v199
	v_lshlrev_b32_e32 v70, 16, v70
	v_mul_f32_e32 v68, 0xbfb8aa3b, v68
	v_exp_f32_e32 v68, v68
	v_mul_f32_e32 v70, v199, v70
	v_cvt_pk_bf16_f32 v70, v70, s0
	ds_write_b16 v67, v70
	v_add_f32_e32 v70, v71, v197
	v_mul_f32_e32 v71, 0x3fb8aa3b, v70
	v_exp_f32_e32 v71, v71
	v_sub_f32_e32 v69, 1.0, v69
	v_mul_f32_e32 v68, v69, v68
	v_lshlrev_b32_e32 v73, 16, v73
	v_cvt_pk_bf16_f32 v68, v68, s0
	ds_write_b16 v67, v68 offset:16384
	v_mul_f32_e32 v67, v71, v73
	v_cvt_pk_bf16_f32 v67, v67, s0
	v_lshl_add_u32 v68, v137, 1, s91
	ds_write_b16 v68, v67 offset:256
	v_mul_f32_e32 v67, 0xbfb8aa3b, v70
	v_exp_f32_e32 v67, v67
	v_add_f32_e32 v69, v74, v197
	v_mul_f32_e32 v70, 0x3fb8aa3b, v69
	v_exp_f32_e32 v70, v70
	v_sub_f32_e32 v72, 1.0, v72
	v_mul_f32_e32 v67, v72, v67
	v_lshlrev_b32_e32 v77, 16, v77
	v_cvt_pk_bf16_f32 v67, v67, s0
	ds_write_b16 v68, v67 offset:16640
	v_mul_f32_e32 v67, v70, v77
	v_cvt_pk_bf16_f32 v67, v67, s0
	v_lshl_add_u32 v68, v138, 1, s91
	ds_write_b16 v68, v67 offset:512
	v_mul_f32_e32 v67, 0xbfb8aa3b, v69
	v_exp_f32_e32 v67, v67
	v_add_f32_e32 v69, v78, v197
	v_mul_f32_e32 v70, 0x3fb8aa3b, v69
	v_exp_f32_e32 v70, v70
	v_sub_f32_e32 v76, 1.0, v76
	v_mul_f32_e32 v67, v76, v67
	v_lshlrev_b32_e32 v81, 16, v81
	v_cvt_pk_bf16_f32 v67, v67, s0
	ds_write_b16 v68, v67 offset:16896
	v_mul_f32_e32 v67, v70, v81
	v_cvt_pk_bf16_f32 v67, v67, s0
	v_lshl_add_u32 v68, v139, 1, s91
	ds_write_b16 v68, v67 offset:768
	v_mul_f32_e32 v67, 0xbfb8aa3b, v69
	v_exp_f32_e32 v67, v67
	v_add_f32_e32 v69, v80, v197
	v_mul_f32_e32 v70, 0x3fb8aa3b, v69
	v_exp_f32_e32 v70, v70
	v_sub_f32_e32 v79, 1.0, v79
	v_mul_f32_e32 v67, v79, v67
	v_lshlrev_b32_e32 v84, 16, v84
	v_cvt_pk_bf16_f32 v67, v67, s0
	ds_write_b16 v68, v67 offset:17152
	v_mul_f32_e32 v67, v70, v84
	v_cvt_pk_bf16_f32 v67, v67, s0
	v_lshl_add_u32 v68, v140, 1, s91
	ds_write_b16 v68, v67 offset:1024
	v_mul_f32_e32 v67, 0xbfb8aa3b, v69
	v_exp_f32_e32 v67, v67
	v_add_f32_e32 v69, v82, v197
	v_mul_f32_e32 v70, 0x3fb8aa3b, v69
	v_exp_f32_e32 v70, v70
	v_sub_f32_e32 v83, 1.0, v83
	v_mul_f32_e32 v67, v83, v67
	v_lshlrev_b32_e32 v87, 16, v87
	v_cvt_pk_bf16_f32 v67, v67, s0
	ds_write_b16 v68, v67 offset:17408
	v_mul_f32_e32 v67, v70, v87
	v_cvt_pk_bf16_f32 v67, v67, s0
	v_lshl_add_u32 v68, v141, 1, s91
	ds_write_b16 v68, v67 offset:1280
	v_mul_f32_e32 v67, 0xbfb8aa3b, v69
	v_exp_f32_e32 v67, v67
	v_add_f32_e32 v69, v85, v197
	v_mul_f32_e32 v70, 0x3fb8aa3b, v69
	v_exp_f32_e32 v70, v70
	v_sub_f32_e32 v86, 1.0, v86
	v_mul_f32_e32 v67, v86, v67
	v_lshlrev_b32_e32 v172, 16, v172
	v_cvt_pk_bf16_f32 v67, v67, s0
	ds_write_b16 v68, v67 offset:17664
	v_mul_f32_e32 v67, v70, v172
	v_cvt_pk_bf16_f32 v67, v67, s0
	v_lshl_add_u32 v68, v142, 1, s91
	ds_write_b16 v68, v67 offset:1536
	v_mul_f32_e32 v67, 0xbfb8aa3b, v69
	v_exp_f32_e32 v67, v67
	v_add_f32_e32 v69, v173, v197
	v_mul_f32_e32 v70, 0x3fb8aa3b, v69
	v_exp_f32_e32 v70, v70
	v_sub_f32_e32 v171, 1.0, v171
	v_mul_f32_e32 v67, v171, v67
	v_lshlrev_b32_e32 v177, 16, v177
	v_cvt_pk_bf16_f32 v67, v67, s0
	ds_write_b16 v68, v67 offset:17920
	v_mul_f32_e32 v67, v70, v177
	v_cvt_pk_bf16_f32 v67, v67, s0
	v_lshl_add_u32 v68, v143, 1, s91
	ds_write_b16 v68, v67 offset:1792
	v_mul_f32_e32 v67, 0xbfb8aa3b, v69
	v_exp_f32_e32 v67, v67
	v_add_f32_e32 v69, v174, v197
	v_mul_f32_e32 v70, 0x3fb8aa3b, v69
	v_exp_f32_e32 v70, v70
	v_sub_f32_e32 v176, 1.0, v176
	v_mul_f32_e32 v67, v176, v67
	v_lshlrev_b32_e32 v179, 16, v179
	v_cvt_pk_bf16_f32 v67, v67, s0
	ds_write_b16 v68, v67 offset:18176
	v_mul_f32_e32 v67, v70, v179
	v_cvt_pk_bf16_f32 v67, v67, s0
	v_lshl_add_u32 v68, v144, 1, s91
	ds_write_b16 v68, v67 offset:2048
	v_mul_f32_e32 v67, 0xbfb8aa3b, v69
	v_exp_f32_e32 v67, v67
	v_add_f32_e32 v69, v175, v197
	v_mul_f32_e32 v70, 0x3fb8aa3b, v69
	v_exp_f32_e32 v70, v70
	v_sub_f32_e32 v178, 1.0, v178
	v_mul_f32_e32 v67, v178, v67
	v_lshlrev_b32_e32 v183, 16, v183
	v_cvt_pk_bf16_f32 v67, v67, s0
	ds_write_b16 v68, v67 offset:18432
	v_mul_f32_e32 v67, v70, v183
	v_cvt_pk_bf16_f32 v67, v67, s0
	v_lshl_add_u32 v68, v145, 1, s91
	ds_write_b16 v68, v67 offset:2304
	v_mul_f32_e32 v67, 0xbfb8aa3b, v69
	v_exp_f32_e32 v67, v67
	v_add_f32_e32 v69, v180, v197
	v_mul_f32_e32 v70, 0x3fb8aa3b, v69
	v_exp_f32_e32 v70, v70
	v_sub_f32_e32 v181, 1.0, v181
; __device__ __forceinline__ float bf2f(bf16_t b) { return __uint_as_float(((unsigned)b) << 16); }
; #define LBAR() do { asm volatile("s_waitcnt lgkmcnt(0)" ::: "memory"); __builtin_amdgcn_s_barrier(); asm volatile("" ::: "memory"); } while (0)
; #define HGO_ISSUE_G(it_) do { const int sh_ = (it_) >> 7, c_ = (it_) & 127, b_ = sh_ >> 3, h_ = sh_ & 7; const bf16_t* pj_ = (const bf16_t*)(ws + WS_PROJ) + ((size_t)b_ * SEQ + (size_t)c_ * 64) * NPROJ; \
;         dma_rows<16>((LAS unsigned char*)GR, pj_ + C_HG + h_ * 128, NPROJ, 16, w, lane); } while (0)
; __device__ __forceinline__ void hg_out_phase(const Params& p, Frame& F) {
;     ...
;         float gv[4][4];
; #pragma unroll
;         for (int i = 0; i < 4; ++i)
; #pragma unroll
;             for (int nb = 0; nb < 4; ++nb) gv[i][nb] = bf2f(GR[(16 * tb + 4 * fq + i) * 128 + 16 * (4 * vh + nb) + fr]);
;         LBAR();
;         if (item + F.G < 2048) HGO_ISSUE_G(item + F.G);
	v_mul_f32_e32 v67, v181, v67
	v_lshlrev_b32_e32 v186, 16, v186
	v_cvt_pk_bf16_f32 v67, v67, s0
	ds_write_b16 v68, v67 offset:18688
	v_mul_f32_e32 v67, v70, v186
	v_cvt_pk_bf16_f32 v67, v67, s0
	v_lshl_add_u32 v68, v146, 1, s91
	ds_write_b16 v68, v67 offset:2560
	v_mul_f32_e32 v67, 0xbfb8aa3b, v69
	v_exp_f32_e32 v67, v67
	v_add_f32_e32 v69, v182, v197
	v_mul_f32_e32 v70, 0x3fb8aa3b, v69
	v_exp_f32_e32 v70, v70
	v_sub_f32_e32 v185, 1.0, v185
	v_mul_f32_e32 v67, v185, v67
	v_lshlrev_b32_e32 v189, 16, v189
	v_cvt_pk_bf16_f32 v67, v67, s0
	ds_write_b16 v68, v67 offset:18944
	v_mul_f32_e32 v67, v70, v189
	v_cvt_pk_bf16_f32 v67, v67, s0
	v_lshl_add_u32 v68, v147, 1, s91
	ds_write_b16 v68, v67 offset:2816
	v_mul_f32_e32 v67, 0xbfb8aa3b, v69
	v_exp_f32_e32 v67, v67
	v_add_f32_e32 v69, v184, v197
	v_mul_f32_e32 v70, 0x3fb8aa3b, v69
	v_exp_f32_e32 v70, v70
	v_sub_f32_e32 v188, 1.0, v188
	v_mul_f32_e32 v67, v188, v67
	v_lshlrev_b32_e32 v192, 16, v192
	v_cvt_pk_bf16_f32 v67, v67, s0
	ds_write_b16 v68, v67 offset:19200
	v_mul_f32_e32 v67, v70, v192
	v_cvt_pk_bf16_f32 v67, v67, s0
	v_lshl_add_u32 v68, v148, 1, s91
	ds_write_b16 v68, v67 offset:3072
	v_mul_f32_e32 v67, 0xbfb8aa3b, v69
	v_exp_f32_e32 v67, v67
	v_add_f32_e32 v69, v187, v197
	v_mul_f32_e32 v70, 0x3fb8aa3b, v69
	v_exp_f32_e32 v70, v70
	v_sub_f32_e32 v191, 1.0, v191
	v_mul_f32_e32 v67, v191, v67
	v_lshlrev_b32_e32 v194, 16, v194
	v_cvt_pk_bf16_f32 v67, v67, s0
	ds_write_b16 v68, v67 offset:19456
	v_mul_f32_e32 v67, v70, v194
	v_cvt_pk_bf16_f32 v67, v67, s0
	v_lshl_add_u32 v68, v149, 1, s91
	ds_write_b16 v68, v67 offset:3328
	v_mul_f32_e32 v67, 0xbfb8aa3b, v69
	v_exp_f32_e32 v67, v67
	v_add_f32_e32 v69, v190, v197
	v_mul_f32_e32 v70, 0x3fb8aa3b, v69
	v_exp_f32_e32 v70, v70
	v_sub_f32_e32 v193, 1.0, v193
	v_mul_f32_e32 v67, v193, v67
	v_lshlrev_b32_e32 v196, 16, v196
	v_cvt_pk_bf16_f32 v67, v67, s0
	ds_write_b16 v68, v67 offset:19712
	v_mul_f32_e32 v67, v70, v196
	v_cvt_pk_bf16_f32 v67, v67, s0
	v_lshl_add_u32 v68, v150, 1, s91
	ds_write_b16 v68, v67 offset:3584
	v_mul_f32_e32 v67, 0xbfb8aa3b, v69
	v_exp_f32_e32 v67, v67
	v_sub_f32_e32 v195, 1.0, v195
	v_add_f32_e32 v69, v75, v197
	v_mul_f32_e32 v70, 0x3fb8aa3b, v69
	v_mul_f32_e32 v67, v195, v67
	v_cvt_pk_bf16_f32 v67, v67, s0
	ds_write_b16 v68, v67 offset:19968
	v_mul_f32_e32 v68, 0xbfb8aa3b, v69
	v_exp_f32_e32 v70, v70
	v_exp_f32_e32 v68, v68
	v_sub_f32_e32 v66, 1.0, v66
	v_lshlrev_b32_e32 v198, 16, v198
	v_mul_f32_e32 v67, v70, v198
	v_mul_f32_e32 v66, v66, v68
	v_cvt_pk_bf16_f32 v67, v67, s0
	v_lshl_add_u32 v69, v151, 1, s91
	v_cvt_pk_bf16_f32 v66, v66, s0
	ds_write_b16 v69, v67 offset:3840
	ds_write_b16 v69, v66 offset:20224
	v_add_u32_e32 v66, s41, v126
	v_add_u32_e32 v67, s42, v126
	v_add_u32_e32 v68, s41, v128
	v_add_u32_e32 v69, s42, v128
	ds_read_u16 v177, v66
	ds_read_u16 v178, v66 offset:32
	ds_read_u16 v179, v66 offset:64
	ds_read_u16 v180, v67
	ds_read_u16 v181, v68
	ds_read_u16 v182, v68 offset:32
	ds_read_u16 v183, v68 offset:64
	ds_read_u16 v184, v69
	v_add_u32_e32 v66, s41, v130
	v_add_u32_e32 v67, s42, v130
	v_add_u32_e32 v68, s41, v132
	v_add_u32_e32 v69, s42, v132
	ds_read_u16 v185, v66
	ds_read_u16 v186, v66 offset:32
	ds_read_u16 v173, v66 offset:64
	ds_read_u16 v174, v67
	ds_read_u16 v175, v68
	ds_read_u16 v176, v68 offset:32
	ds_read_u16 v171, v68 offset:64
	ds_read_u16 v172, v69
	s_waitcnt lgkmcnt(0)
	s_barrier
	s_mov_b32 s99, 0
	s_andn2_b64 vcc, exec, s[94:95]
	v_readlane_b32 s94, v245, 56
	s_cbranch_vccnz .LBB0_581
	v_mov_b32_e32 v66, v162
	s_and_b64 vcc, exec, s[38:39]
	s_cbranch_vccnz .LBB0_581
	s_mov_b32 s99, 1
	s_ashr_i32 s0, s66, 10
	s_mul_hi_i32 s1, s0, 0x7000000
	s_mul_i32 s0, s0, 0x7000000
	v_ashrrev_i32_e32 v67, 31, v66
	s_add_u32 s0, s0, s64
	v_lshrrev_b32_e32 v67, 28, v67
	s_addc_u32 s1, s1, 0
	v_add_u32_e32 v67, v66, v67
	s_add_u32 s0, s67, s0
	v_ashrrev_i32_e32 v68, 4, v67
	v_and_b32_e32 v67, 0x1ffffff0, v67
	s_addc_u32 s1, 0, s1
	v_sub_u32_e32 v66, v66, v67
	v_add_u32_e32 v70, s78, v68
	v_mov_b64_e32 v[68:69], s[0:1]
	v_lshlrev_b32_e32 v66, 3, v66
	v_mad_i64_i32 v[68:69], s[0:1], v70, s80, v[68:69]
	v_ashrrev_i32_e32 v67, 31, v66
	v_readlane_b32 s0, v244, 20
	v_lshl_add_u64 v[66:67], v[66:67], 1, v[68:69]
	v_readlane_b32 s1, v244, 21
	v_mov_b32_e32 v68, s79
	s_nop 0
	v_lshl_add_u64 v[66:67], s[0:1], 0, v[66:67]
	v_readlane_b32 s0, v244, 22

; #define LAS __attribute__((address_space(3)))
; __device__ __forceinline__ bf16_t f2bf(float v) { return (bf16_t)(cvt_pk_bf16(v, 0.f) & 0xffffu); }
; __device__ __forceinline__ void hg_out_phase(const Params& p, Frame& F) {
;     ...
;         bf16x8 aq[4];
; #pragma unroll
;         for (int ks = 0; ks < 4; ++ks) aq[ks] = *(const LAS bf16x8*)(QR + (16 * tb + fr) * 128 + (((4 * ks + fq) ^ fr) << 3));
; #pragma unroll
;         for (int sb = 0; sb < 4; ++sb) {
;             f32x4 acc = (f32x4){0.f, 0.f, 0.f, 0.f};
;             if (sb <= tb) {
; #pragma unroll
;                 for (int ks = 0; ks < 4; ++ks) acc = __builtin_amdgcn_mfma_f32_16x16x32_bf16(aq[ks], *(const LAS bf16x8*)(ZR + (16 * sb + fr) * 128 + (((4 * ks + fq) ^ fr) << 3)), acc, 0, 0, 0);
;             }
; #pragma unroll
;             for (int i = 0; i < 4; ++i) { const int tl = 16 * tb + 4 * fq + i, s = 16 * sb + fr; ATT[(4 * fq + i) * TT + s] = f2bf((s <= tl) ? acc[i] : 0.f); }
;         }
;         f32x4 o[4];
; #pragma unroll
;         for (int nb = 0; nb < 4; ++nb) { o[nb] = (f32x4){0.f, 0.f, 0.f, 0.f};
; #pragma unroll
;             for (int ks = 0; ks < 4; ++ks) o[nb] = __builtin_amdgcn_mfma_f32_16x16x32_bf16(aq[ks], stf[nb][ks], o[nb], 0, 0, 0); }
;         asm volatile("s_waitcnt lgkmcnt(0)" ::: "memory");
;         bf16x8 aa[2];
; #pragma unroll
;         for (int ks = 0; ks < 2; ++ks) aa[ks] = lds_frag(ATT, fr, TT, 32 * ks + 8 * fq);
; #pragma unroll
;         for (int nb = 0; nb < 4; ++nb) { const int vrow = 16 * (4 * vh + nb) + fr;
; #pragma unroll
;             for (int ks = 0; ks < 2; ++ks) o[nb] = __builtin_amdgcn_mfma_f32_16x16x32_bf16(aa[ks], lds_frag(VT, vrow, TT, 32 * ks + 8 * fq), o[nb], 0, 0, 0); }
;         float sq[4];
; #pragma unroll
;         for (int i = 0; i < 4; ++i) { float s = 0.f;
; #pragma unroll
;             for (int nb = 0; nb < 4; ++nb) s += o[nb][i] * o[nb][i];
;             s += __shfl_xor(s, 1); s += __shfl_xor(s, 2); s += __shfl_xor(s, 4); s += __shfl_xor(s, 8); sq[i] = s; }
;         if (fr == 0) {
; #pragma unroll
;             for (int i = 0; i < 4; ++i) ssqp[vh * 64 + 16 * tb + 4 * fq + i] = sq[i]; }
.LBB0_591:
	s_cmp_lg_u32 s99, 0
	s_cbranch_scc1 .Lhgo_w2
	s_waitcnt vmcnt(0)
	s_branch .Lhgo_wd
.Lhgo_w2:
	s_waitcnt vmcnt(2)
.Lhgo_wd:
	v_mfma_f32_16x16x32_bf16 v[30:33], v[74:77], v[30:33], 0
	s_nop 5
	v_cvt_pk_bf16_f32 v82, v82, s0
	v_cndmask_b32_e64 v82, v82, 0, s[28:29]
	ds_write_b16 v164, v82 offset:96
	v_mfma_f32_16x16x32_bf16 v[30:33], v[66:69], v[34:37], v[30:33]
	v_cvt_pk_bf16_f32 v82, v83, s0
	v_cndmask_b32_e64 v82, v82, 0, s[30:31]
	ds_write_b16 v164, v82 offset:240
	v_mfma_f32_16x16x32_bf16 v[30:33], v[70:73], v[38:41], v[30:33]
	v_cvt_pk_bf16_f32 v82, v84, s0
	v_cndmask_b32_e64 v82, v82, 0, s[34:35]
	ds_write_b16 v164, v82 offset:384
	v_mfma_f32_16x16x32_bf16 v[38:41], v[74:77], v[62:65], 0
	v_cvt_pk_bf16_f32 v82, v85, s0
	v_cndmask_b32_e64 v82, v82, 0, s[36:37]
	ds_write_b16 v164, v82 offset:528
	v_mfma_f32_16x16x32_bf16 v[14:17], v[74:77], v[14:17], 0
	s_waitcnt lgkmcnt(0)
	v_mfma_f32_16x16x32_bf16 v[26:29], v[66:69], v[26:29], v[38:41]
	v_mfma_f32_16x16x32_bf16 v[2:5], v[66:69], v[2:5], v[14:17]
	v_mfma_f32_16x16x32_bf16 v[22:25], v[70:73], v[22:25], v[26:29]
	v_mfma_f32_16x16x32_bf16 v[34:37], v[74:77], v[46:49], 0
	v_mfma_f32_16x16x32_bf16 v[2:5], v[70:73], v[6:9], v[2:5]
	v_add_u32_e32 v6, v123, v124
	v_mfma_f32_16x16x32_bf16 v[18:21], v[78:81], v[18:21], v[22:25]
	s_nop 3
	ds_read_b128 v[22:25], v6
	ds_read_b128 v[26:29], v6 offset:64
	ds_read_b128 v[6:9], v154
	v_mfma_f32_16x16x32_bf16 v[30:33], v[78:81], v[42:45], v[30:33]
	v_mfma_f32_16x16x32_bf16 v[34:37], v[66:69], v[50:53], v[34:37]
	v_mfma_f32_16x16x32_bf16 v[2:5], v[78:81], v[10:13], v[2:5]
	ds_read_b128 v[10:13], v154 offset:64
	s_waitcnt lgkmcnt(1)
	v_mfma_f32_16x16x32_bf16 v[6:9], v[22:25], v[6:9], v[30:33]
	v_mfma_f32_16x16x32_bf16 v[34:37], v[70:73], v[54:57], v[34:37]
	s_waitcnt lgkmcnt(0)
	v_mfma_f32_16x16x32_bf16 v[14:17], v[26:29], v[10:13], v[6:9]
	ds_read_b128 v[10:13], v155 offset:64
	s_nop 3
	ds_read_b128 v[6:9], v155
	v_mfma_f32_16x16x32_bf16 v[34:37], v[78:81], v[58:61], v[34:37]
	s_waitcnt lgkmcnt(0)
	v_mfma_f32_16x16x32_bf16 v[6:9], v[22:25], v[6:9], v[34:37]
	v_mfma_f32_16x16x32_bf16 v[6:9], v[26:29], v[10:13], v[6:9]
	ds_read_b128 v[10:13], v156
	s_waitcnt lgkmcnt(0)
	v_mfma_f32_16x16x32_bf16 v[10:13], v[22:25], v[10:13], v[18:21]
	s_nop 2
	ds_read_b128 v[18:21], v156 offset:64
	s_waitcnt lgkmcnt(0)
	v_mfma_f32_16x16x32_bf16 v[10:13], v[26:29], v[18:21], v[10:13]
	ds_read_b128 v[18:21], v157
	s_waitcnt lgkmcnt(0)
	v_mfma_f32_16x16x32_bf16 v[2:5], v[22:25], v[18:21], v[2:5]
	ds_read_b128 v[18:21], v157 offset:64
	s_waitcnt lgkmcnt(0)
	v_mfma_f32_16x16x32_bf16 v[2:5], v[26:29], v[18:21], v[2:5]
	v_and_b32_e32 v19, 64, v158
	v_xor_b32_e32 v18, 1, v158
	v_add_u32_e32 v19, 64, v19
	v_cmp_lt_i32_e32 vcc, v18, v19
	v_pk_mul_f32 v[20:21], v[6:7], v[6:7]
	s_nop 0
	v_cndmask_b32_e32 v18, v158, v18, vcc
	v_lshlrev_b32_e32 v25, 2, v18
	v_xor_b32_e32 v18, 2, v158
	v_cmp_lt_i32_e32 vcc, v18, v19
	v_pk_fma_f32 v[20:21], v[14:15], v[14:15], v[20:21]
	s_nop 0
	v_cndmask_b32_e32 v18, v158, v18, vcc
	v_lshlrev_b32_e32 v26, 2, v18
	v_xor_b32_e32 v18, 4, v158
	v_cmp_lt_i32_e32 vcc, v18, v19
	v_pk_fma_f32 v[20:21], v[10:11], v[10:11], v[20:21]
	s_nop 0
	v_cndmask_b32_e32 v18, v158, v18, vcc
	v_lshlrev_b32_e32 v27, 2, v18
	v_xor_b32_e32 v18, 8, v158
	v_cmp_lt_i32_e32 vcc, v18, v19
	s_nop 1
	v_cndmask_b32_e32 v18, v158, v18, vcc
	v_lshlrev_b32_e32 v28, 2, v18
	v_pk_mul_f32 v[18:19], v[8:9], v[8:9]
	s_nop 0
	v_pk_fma_f32 v[18:19], v[16:17], v[16:17], v[18:19]
	s_nop 0
	v_pk_fma_f32 v[18:19], v[12:13], v[12:13], v[18:19]
	s_nop 0
	v_pk_fma_f32 v[22:23], v[4:5], v[4:5], v[18:19]
	v_pk_fma_f32 v[18:19], v[2:3], v[2:3], v[20:21]
	ds_bpermute_b32 v20, v25, v18
	ds_bpermute_b32 v21, v25, v19
	ds_bpermute_b32 v24, v25, v22
	ds_bpermute_b32 v25, v25, v23
	s_waitcnt lgkmcnt(2)
	v_pk_add_f32 v[18:19], v[18:19], v[20:21]
	ds_bpermute_b32 v20, v26, v18
	s_waitcnt lgkmcnt(1)
	v_pk_add_f32 v[22:23], v[22:23], v[24:25]
	ds_bpermute_b32 v21, v26, v19
	ds_bpermute_b32 v24, v26, v22
	ds_bpermute_b32 v25, v26, v23
	s_waitcnt lgkmcnt(2)
	v_pk_add_f32 v[18:19], v[18:19], v[20:21]
	ds_bpermute_b32 v20, v27, v18
	s_waitcnt lgkmcnt(1)
	v_pk_add_f32 v[22:23], v[22:23], v[24:25]
	ds_bpermute_b32 v21, v27, v19
	ds_bpermute_b32 v24, v27, v22
	ds_bpermute_b32 v25, v27, v23
	s_waitcnt lgkmcnt(2)
	v_pk_add_f32 v[18:19], v[18:19], v[20:21]
	ds_bpermute_b32 v20, v28, v18
	s_waitcnt lgkmcnt(1)
	v_pk_add_f32 v[22:23], v[22:23], v[24:25]
	ds_bpermute_b32 v21, v28, v19
	ds_bpermute_b32 v24, v28, v22
	ds_bpermute_b32 v25, v28, v23
	s_and_saveexec_b64 s[0:1], s[2:3]
	s_cbranch_execz .LBB0_560
	v_readlane_b32 s33, v245, 63
	s_waitcnt lgkmcnt(2)
	v_pk_add_f32 v[18:19], v[18:19], v[20:21]
	v_add_u32_e32 v20, s33, v162
	ds_write2_b32 v20, v18, v19 offset1:1
	s_waitcnt lgkmcnt(1)
	v_pk_add_f32 v[18:19], v[22:23], v[24:25]
	ds_write2_b32 v20, v18, v19 offset0:2 offset1:3
	s_branch .LBB0_560

; #define LAS __attribute__((address_space(3)))
; #define VLBAR() do { asm volatile("s_waitcnt vmcnt(0) lgkmcnt(0)" ::: "memory"); __builtin_amdgcn_s_barrier(); asm volatile("" ::: "memory"); } while (0)
; __device__ __forceinline__ void ml_out_phase(const Params& p, Frame& F) {
;     ...
;         VLBAR();
;         if (tid < 256) nwl[tid] = nwx;
;         f32x4 nsv[8]; bf16x8 ctf[4][4], ctg[4][4];
;         { const bf16_t* CT = (const bf16_t*)(ws + WS_CST) + (size_t)item * 32768;
; #pragma unroll
;           for (int nb = 0; nb < 4; ++nb)
; #pragma unroll
;               for (int ks = 0; ks < 4; ++ks) ctf[nb][ks] = *(const bf16x8*)(CT + (size_t)(16 * (8 * vh + nb) + fr) * 128 + 32 * ks + 8 * fq); }
;         __builtin_amdgcn_sched_barrier(0);
;         if (w == 0) {
;             float g = lf;
; #pragma unroll
;             for (int o = 1; o < 64; o <<= 1) { const float v = __shfl_up(g, o); if (lane >= o) g += v; }
;             const float a = li - g; float pm = a;
; #pragma unroll
;             for (int o = 1; o < 64; o <<= 1) { const float v = __shfl_up(pm, o); if (lane >= o) pm = fmaxf(pm, v); }
;             const float M = fmaxf(mst, pm);
;             int ln = lane; asm volatile("" : "+v"(ln)); LAS float* gs = avec + ln;
;             gs[0] = a; gs[64] = M; gs[128] = __expf(mst - M); gs[192] = __expf(-(g + M));
;         }
.LBB0_609:
	s_waitcnt vmcnt(0) lgkmcnt(0)
	s_barrier
	s_mov_b64 s[0:1], exec
	v_readlane_b32 s4, v245, 19
	v_readlane_b32 s5, v245, 20
	s_and_b64 s[4:5], s[0:1], s[4:5]
	s_mov_b64 exec, s[4:5]
	s_cbranch_execz .LBB0_611
	ds_write_b32 v157, v181
.LBB0_611:
	s_or_b64 exec, exec, s[0:1]
	s_ashr_i32 s91, s90, 31
	s_lshl_b64 s[0:1], s[90:91], 16
	v_lshl_add_u64 v[152:153], v[132:133], 0, s[0:1]
	v_lshl_add_u64 v[2:3], v[152:153], 0, v[134:135]
	global_load_dwordx4 v[62:65], v[2:3], off
	global_load_dwordx4 v[58:61], v[2:3], off offset:64
	global_load_dwordx4 v[54:57], v[2:3], off offset:128
	global_load_dwordx4 v[50:53], v[2:3], off offset:192
	v_lshl_add_u64 v[2:3], v[152:153], 0, v[136:137]
	global_load_dwordx4 v[46:49], v[2:3], off
	global_load_dwordx4 v[42:45], v[2:3], off offset:64
	global_load_dwordx4 v[38:41], v[2:3], off offset:128
	global_load_dwordx4 v[34:37], v[2:3], off offset:192
	v_lshl_add_u64 v[2:3], v[152:153], 0, v[138:139]
	global_load_dwordx4 v[30:33], v[2:3], off
	global_load_dwordx4 v[26:29], v[2:3], off offset:64
	global_load_dwordx4 v[22:25], v[2:3], off offset:128
	global_load_dwordx4 v[18:21], v[2:3], off offset:192
	v_lshl_add_u64 v[2:3], v[152:153], 0, v[140:141]
	global_load_dwordx4 v[14:17], v[2:3], off
	global_load_dwordx4 v[10:13], v[2:3], off offset:64
	global_load_dwordx4 v[6:9], v[2:3], off offset:128
	s_nop 0
	global_load_dwordx4 v[2:5], v[2:3], off offset:192
	s_andn2_b64 vcc, exec, s[16:17]
	v_mbcnt_hi_u32_b32 v128, -1, v223
	s_cbranch_vccnz .LBB0_613
	v_and_b32_e32 v66, 64, v128
	v_add_u32_e32 v67, -1, v128
	v_cmp_lt_i32_e32 vcc, v67, v66
	v_add_u32_e32 v69, -2, v128
	v_readlane_b32 s0, v244, 16
	v_cndmask_b32_e32 v67, v67, v128, vcc
	v_lshlrev_b32_e32 v67, 2, v67
	ds_bpermute_b32 v68, v67, v155
	v_cmp_lt_i32_e32 vcc, v69, v66
	v_readlane_b32 s1, v244, 17
	v_readlane_b32 s4, v244, 18
	v_cndmask_b32_e32 v69, v69, v128, vcc
	s_waitcnt lgkmcnt(0)
	v_add_f32_e32 v68, v155, v68
	v_cndmask_b32_e64 v68, v68, v155, s[0:1]
	v_lshlrev_b32_e32 v69, 2, v69
	ds_bpermute_b32 v70, v69, v68
	v_readlane_b32 s5, v244, 19
	v_readlane_b32 s20, v244, 20
	v_readlane_b32 s21, v244, 21
	s_mov_b32 s13, s23
	s_waitcnt lgkmcnt(0)
	v_add_f32_e32 v70, v68, v70
	v_cndmask_b32_e64 v68, v70, v68, s[4:5]
	v_add_u32_e32 v70, -4, v128
	v_cmp_lt_i32_e32 vcc, v70, v66
	v_readlane_b32 s22, v244, 22
	v_readlane_b32 s23, v244, 23
	v_cndmask_b32_e32 v70, v70, v128, vcc
	v_lshlrev_b32_e32 v70, 2, v70
	ds_bpermute_b32 v71, v70, v68
	v_readlane_b32 s24, v245, 59
	v_readlane_b32 s25, v245, 60
	s_waitcnt lgkmcnt(0)
	v_add_f32_e32 v71, v68, v71
	v_cndmask_b32_e64 v68, v71, v68, s[20:21]
	v_add_u32_e32 v71, -8, v128
	v_cmp_lt_i32_e32 vcc, v71, v66
	s_nop 1
	v_cndmask_b32_e32 v71, v71, v128, vcc
	v_lshlrev_b32_e32 v71, 2, v71
	ds_bpermute_b32 v72, v71, v68
	s_waitcnt lgkmcnt(0)
	v_add_f32_e32 v72, v68, v72
	v_cndmask_b32_e64 v68, v72, v68, s[22:23]
	v_add_u32_e32 v72, -16, v128
	v_cmp_lt_i32_e32 vcc, v72, v66
	s_nop 1
	v_cndmask_b32_e32 v72, v72, v128, vcc
	v_lshlrev_b32_e32 v72, 2, v72
	ds_bpermute_b32 v73, v72, v68
	s_waitcnt lgkmcnt(0)
	v_add_f32_e32 v73, v68, v73
	v_cndmask_b32_e64 v68, v73, v68, s[2:3]
	v_subrev_u32_e32 v73, 32, v128
	v_cmp_lt_i32_e32 vcc, v73, v66
	s_nop 1
	v_cndmask_b32_e32 v66, v73, v128, vcc
	v_lshlrev_b32_e32 v66, 2, v66
	ds_bpermute_b32 v73, v66, v68
	s_waitcnt lgkmcnt(0)
	v_add_f32_e32 v73, v68, v73
	v_cndmask_b32_e64 v68, v73, v68, s[24:25]
	v_sub_f32_e32 v73, v154, v68
	ds_bpermute_b32 v67, v67, v73
	s_waitcnt lgkmcnt(0)
	v_max_f32_e32 v67, v67, v67
	v_max_f32_e32 v67, v73, v67
	v_cndmask_b32_e64 v67, v67, v73, s[0:1]
	ds_bpermute_b32 v69, v69, v67
	s_waitcnt lgkmcnt(0)
	v_max_f32_e32 v69, v69, v69
	v_max_f32_e32 v69, v67, v69
	v_cndmask_b32_e64 v67, v69, v67, s[4:5]
	ds_bpermute_b32 v69, v70, v67
	s_waitcnt lgkmcnt(0)
	v_max_f32_e32 v69, v69, v69
	v_max_f32_e32 v69, v67, v69
	v_cndmask_b32_e64 v67, v69, v67, s[20:21]
	ds_bpermute_b32 v69, v71, v67
	s_waitcnt lgkmcnt(0)
	v_max_f32_e32 v69, v69, v69
	v_max_f32_e32 v69, v67, v69
	v_cndmask_b32_e64 v67, v69, v67, s[22:23]
	ds_bpermute_b32 v69, v72, v67
	s_mov_b32 s23, s13
	s_waitcnt lgkmcnt(0)
	v_max_f32_e32 v69, v69, v69
	v_max_f32_e32 v69, v67, v69
	v_cndmask_b32_e64 v67, v69, v67, s[2:3]
	ds_bpermute_b32 v66, v66, v67
	v_max_f32_e32 v69, v67, v67
	s_waitcnt lgkmcnt(0)
	v_max_f32_e32 v66, v66, v66
	v_max_f32_e32 v66, v69, v66
	v_cndmask_b32_e64 v66, v66, v67, s[24:25]
	v_max_f32_e32 v66, v66, v66
	v_max_f32_e32 v67, v156, v156
	v_max_f32_e32 v66, v67, v66
	v_mov_b32_e32 v67, v162
	v_sub_f32_e32 v69, v156, v66
	v_lshl_add_u32 v67, v67, 2, 0
	v_add_u32_e32 v67, 0x1e000, v67
	ds_write2st64_b32 v67, v73, v66 offset1:1
	v_add_f32_e32 v66, v68, v66
	v_mul_f32_e32 v69, 0x3fb8aa3b, v69
	v_mul_f32_e32 v66, 0xbfb8aa3b, v66
	v_exp_f32_e32 v69, v69
	v_exp_f32_e32 v66, v66
	ds_write2st64_b32 v67, v69, v66 offset0:2 offset1:3
; #define LAS __attribute__((address_space(3)))
; __device__ __forceinline__ float bf2f(bf16_t b) { return __uint_as_float(((unsigned)b) << 16); }
; #define LBAR() do { asm volatile("s_waitcnt lgkmcnt(0)" ::: "memory"); __builtin_amdgcn_s_barrier(); asm volatile("" ::: "memory"); } while (0)
; #define MLO_ISSUE_V(it_, col_) do { const int sh_ = (it_) >> 7, c_ = (it_) & 127, b_ = sh_ >> 2, h_ = sh_ & 3; const bf16_t* pj_ = (const bf16_t*)(ws + WS_PROJ) + ((size_t)b_ * SEQ + (size_t)c_ * 64) * NPROJ; \
;         dma_rows<32>((LAS unsigned char*)VR, pj_ + (col_) + h_ * 256, NPROJ, 32, w, lane); } while (0)
; __device__ __forceinline__ void ml_out_phase(const Params& p, Frame& F) {
;     ...
;         { const int v = tid & 255, hf = tid >> 8; unsigned pk[16];
; #pragma unroll
;           for (int j = 0; j < 16; ++j) pk[j] = (unsigned)VR[(32 * hf + 2 * j) * 256 + v] | ((unsigned)VR[(32 * hf + 2 * j + 1) * 256 + v] << 16);
; #pragma unroll
;           for (int q = 0; q < 4; ++q) *(LAS u32x4*)(VT + v * TT + 32 * hf + 8 * q) = (u32x4){pk[4 * q], pk[4 * q + 1], pk[4 * q + 2], pk[4 * q + 3]}; }
;         const int d = tid & 127, tq = w >> 1;
;         float rq[19], rk[19];
; #pragma unroll
;         for (int j = 0; j < 19; ++j) { const bool z = (c == 0 && 16 * tq + j < 3); const float a = bf2f(QR[(16 * tq + j) * 128 + d]), bb = bf2f(KR[(16 * tq + j) * 128 + d]); rq[j] = z ? 0.f : a; rk[j] = z ? 0.f : bb; }
;         LBAR();
;         MLO_ISSUE_V(item, C_MO);
.LBB0_613:
	ds_read_u16 v66, v159 offset:34816
	ds_read_u16 v67, v159 offset:35328
	ds_read_u16 v68, v159 offset:35840
	ds_read_u16 v69, v159 offset:36352
	ds_read_u16 v70, v159 offset:36864
	ds_read_u16 v71, v159 offset:37376
	ds_read_u16 v72, v159 offset:37888
	ds_read_u16 v73, v159 offset:38400
	s_waitcnt lgkmcnt(0)
	v_lshl_or_b32 v66, v67, 16, v66
	v_lshl_or_b32 v67, v69, 16, v68
	v_lshl_or_b32 v68, v71, 16, v70
	ds_read_u16 v70, v159 offset:38912
	ds_read_u16 v71, v159 offset:39424
	ds_read_u16 v74, v159 offset:39936
	ds_read_u16 v75, v159 offset:40448
	ds_read_u16 v76, v159 offset:40960
	ds_read_u16 v77, v159 offset:41472
	ds_read_u16 v78, v159 offset:41984
	ds_read_u16 v79, v159 offset:42496
	v_lshl_or_b32 v69, v73, 16, v72
	s_waitcnt lgkmcnt(6)
	v_lshl_or_b32 v70, v71, 16, v70
	s_waitcnt lgkmcnt(4)
	v_lshl_or_b32 v71, v75, 16, v74
	s_waitcnt lgkmcnt(2)
	v_lshl_or_b32 v72, v77, 16, v76
	s_waitcnt lgkmcnt(0)
	v_lshl_or_b32 v73, v79, 16, v78
	ds_read_u16 v74, v159 offset:43008
	ds_read_u16 v75, v159 offset:43520
	ds_read_u16 v76, v159 offset:44032
	ds_read_u16 v77, v159 offset:44544
	ds_read_u16 v78, v159 offset:45056
	ds_read_u16 v79, v159 offset:45568
	ds_read_u16 v80, v159 offset:46080
	ds_read_u16 v81, v159 offset:46592
	s_waitcnt lgkmcnt(6)
	v_lshl_or_b32 v74, v75, 16, v74
	s_waitcnt lgkmcnt(4)
	v_lshl_or_b32 v75, v77, 16, v76
	s_waitcnt lgkmcnt(2)
	v_lshl_or_b32 v76, v79, 16, v78
	ds_read_u16 v78, v159 offset:47104
	ds_read_u16 v79, v159 offset:47616
	ds_read_u16 v82, v159 offset:48128
	ds_read_u16 v83, v159 offset:48640
	ds_read_u16 v84, v159 offset:49152
	ds_read_u16 v85, v159 offset:49664
	ds_read_u16 v86, v159 offset:50176
	ds_read_u16 v87, v159 offset:50688
	s_waitcnt lgkmcnt(8)
	v_lshl_or_b32 v77, v81, 16, v80
	s_waitcnt lgkmcnt(6)
	v_lshl_or_b32 v78, v79, 16, v78
	s_waitcnt lgkmcnt(4)
	v_lshl_or_b32 v79, v83, 16, v82
	s_waitcnt lgkmcnt(2)
	v_lshl_or_b32 v80, v85, 16, v84
	s_waitcnt lgkmcnt(0)
	v_lshl_or_b32 v81, v87, 16, v86
	ds_write_b128 v217, v[66:69]
	ds_write_b128 v217, v[70:73] offset:16
	ds_write_b128 v217, v[74:77] offset:32
	ds_write_b128 v217, v[78:81] offset:48
	ds_read_u16 v85, v176
	ds_read_u16 v81, v176 offset:256
	ds_read_u16 v73, v176 offset:512
	ds_read_u16 v68, v176 offset:768
	ds_read_u16 v69, v176 offset:1024
	ds_read_u16 v70, v176 offset:1280
	ds_read_u16 v71, v176 offset:1536
	ds_read_u16 v72, v176 offset:1792
	ds_read_u16 v80, v176 offset:18688
	ds_read_u16 v79, v176 offset:18944
	ds_read_u16 v74, v176 offset:19200
	ds_read_u16 v75, v176 offset:19456
	ds_read_u16 v76, v176 offset:19712
	ds_read_u16 v77, v176 offset:19968
	ds_read_u16 v78, v176 offset:20224
	ds_read_u16 v94, v176 offset:20480
	ds_read_u16 v84, v176 offset:2048
	ds_read_u16 v83, v176 offset:2304
	ds_read_u16 v82, v176 offset:2560
	ds_read_u16 v99, v176 offset:2816
	ds_read_u16 v98, v176 offset:3072
	ds_read_u16 v95, v176 offset:3328
	ds_read_u16 v96, v176 offset:3584
	ds_read_u16 v97, v176 offset:3840
	ds_read_u16 v90, v176 offset:17408
	ds_read_u16 v89, v176 offset:17664
	ds_read_u16 v88, v176 offset:17920
	ds_read_u16 v87, v176 offset:18176
	ds_read_u16 v86, v176 offset:18432
	ds_read_u16 v100, v176 offset:4096
	ds_read_u16 v101, v176 offset:4352
	ds_read_u16 v102, v176 offset:4608
	ds_read_u16 v108, v176 offset:20736
	ds_read_u16 v107, v176 offset:20992
	ds_read_u16 v106, v176 offset:21248
	ds_read_u16 v105, v176 offset:21504
	ds_read_u16 v104, v176 offset:21760
	ds_read_u16 v103, v176 offset:22016
	s_waitcnt lgkmcnt(0)
	s_barrier
	s_lshl_b32 s0, s72, 1
	s_ashr_i32 s74, s90, 9
	v_cndmask_b32_e64 v67, 0, 1, s[76:77]
	s_and_b32 s58, s54, 0x7f
	s_and_b32 s22, s0, 0x600
	s_ashr_i32 s75, s74, 31
	v_mov_b32_e32 v66, v162
	v_cmp_ne_u32_e64 s[60:61], 1, v67
	s_andn2_b64 vcc, exec, s[76:77]
	s_cbranch_vccnz .LBB0_616
	v_ashrrev_i32_e32 v67, 31, v66
	s_mul_i32 s0, s58, 0xe0000
	v_lshrrev_b32_e32 v67, 27, v67
	s_mul_i32 s4, s74, 0x7000000
	v_add_u32_e32 v67, v66, v67
	s_mul_hi_i32 s1, s74, 0x7000000
	s_add_u32 s0, s4, s0
	v_ashrrev_i32_e32 v91, 5, v67
	v_and_b32_e32 v67, 0x1fffffe0, v67
	s_addc_u32 s1, s1, 0
	v_readlane_b32 s4, v245, 63
	v_sub_u32_e32 v66, v66, v67
	v_mov_b64_e32 v[92:93], s[0:1]
	v_add_u32_e32 v91, s4, v91
	s_movk_i32 s0, 0x3800
	v_lshlrev_b32_e32 v66, 3, v66
	v_mad_i64_i32 v[92:93], s[0:1], v91, s0, v[92:93]
	v_ashrrev_i32_e32 v67, 31, v66
	v_or_b32_e32 v92, s22, v92
	v_readlane_b32 s0, v244, 11
	v_lshl_add_u64 v[66:67], v[66:67], 1, v[92:93]
	v_readlane_b32 s1, v244, 12
	s_nop 1
	v_lshl_add_u64 v[66:67], s[0:1], 0, v[66:67]
	v_readlane_b32 s0, v245, 61
	s_mov_b32 s1, s55

; #define LAS __attribute__((address_space(3)))
; __device__ __forceinline__ float bflo(unsigned w) { return __uint_as_float(w << 16); }
; __device__ __forceinline__ float bfhi(unsigned w) { return __uint_as_float(w & 0xffff0000u); }
; __device__ __forceinline__ bf16_t f2bf(float v) { return (bf16_t)(cvt_pk_bf16(v, 0.f) & 0xffffu); }
; __device__ __forceinline__ void ml_out_phase(const Params& p, Frame& F) {
;     ...
;         for (int sb = 0; sb < 4; ++sb) {
;             f32x4 acc = (f32x4){0.f, 0.f, 0.f, 0.f};
;             if (sb <= tb) {
; #pragma unroll
;                 for (int ks = 0; ks < 4; ++ks) acc = __builtin_amdgcn_mfma_f32_16x16x32_bf16(aq[ks], *(const LAS bf16x8*)(KR + (16 * sb + fr) * 128 + (((4 * ks + fq) ^ fr) << 3)), acc, 0, 0, 0);
;             }
;             const int s = 16 * sb + fr; const float as = avec[s];
; #pragma unroll
;             for (int i = 0; i < 4; ++i) { const int tl = 16 * tb + 4 * fq + i; const float v = (s <= tl) ? acc[i] * __expf(as - Mr[i]) : 0.f; rsum[i] += v; ATT[(4 * fq + i) * TT + s] = f2bf(v); }
;         }
; #pragma unroll
;         for (int i = 0; i < 4; ++i) { float s = rsum[i]; s += __shfl_xor(s, 1); s += __shfl_xor(s, 2); s += __shfl_xor(s, 4); s += __shfl_xor(s, 8); rsum[i] = s; }
;         f32x4 o[8];
; #pragma unroll
;         for (int nb = 0; nb < 4; ++nb) { o[nb] = (f32x4){0.f, 0.f, 0.f, 0.f};
; #pragma unroll
;             for (int ks = 0; ks < 4; ++ks) o[nb] = __builtin_amdgcn_mfma_f32_16x16x32_bf16(aq[ks], ctf[nb][ks], o[nb], 0, 0, 0);
; #pragma unroll
;             for (int i = 0; i < 4; ++i) o[nb][i] *= wi[i]; }
;         { float s = 0.f;
; #pragma unroll
;           for (int ks = 0; ks < 4; ++ks) { const f32x4 n0 = nsv[2 * ks], n1 = nsv[2 * ks + 1];
;               const unsigned* aw = (const unsigned*)&aq[ks];
;               s += bflo(aw[0]) * n0[0] + bfhi(aw[0]) * n0[1] + bflo(aw[1]) * n0[2] + bfhi(aw[1]) * n0[3] + bflo(aw[2]) * n1[0] + bfhi(aw[2]) * n1[1] + bflo(aw[3]) * n1[2] + bfhi(aw[3]) * n1[3]; }
;           s += __shfl_xor(s, 16); s += __shfl_xor(s, 32);
;           if (fq == 0) qnl[w * 16 + fr] = s; }
.LBB0_623:
	v_add_f32_e32 v225, 0, v229
	ds_read_b32 v229, v201
	v_add_f32_e32 v225, v225, v233
	v_add_f32_e32 v225, v225, v237
	v_add_f32_e32 v226, 0, v230
	v_add_f32_e32 v226, v226, v234
	s_waitcnt lgkmcnt(0)
	v_sub_f32_e32 v118, v229, v118
	v_mul_f32_e32 v118, 0x3fb8aa3b, v118
	v_exp_f32_e32 v118, v118
	v_sub_f32_e32 v119, v229, v119
	v_mul_f32_e32 v119, 0x3fb8aa3b, v119
	v_exp_f32_e32 v119, v119
	v_mul_f32_e32 v118, v122, v118
	v_cndmask_b32_e64 v118, v118, 0, s[50:51]
	v_add_f32_e32 v122, v225, v118
	v_cvt_pk_bf16_f32 v118, v118, s0
	ds_write_b16 v224, v118 offset:96
	v_mul_f32_e32 v118, v123, v119
	v_sub_f32_e32 v119, v229, v120
	v_mul_f32_e32 v119, 0x3fb8aa3b, v119
	v_exp_f32_e32 v119, v119
	v_add_f32_e32 v226, v226, v238
	v_cndmask_b32_e64 v118, v118, 0, s[70:71]
	v_add_f32_e32 v123, v226, v118
	v_cvt_pk_bf16_f32 v118, v118, s0
	ds_write_b16 v224, v118 offset:240
	v_mul_f32_e32 v118, v124, v119
	v_sub_f32_e32 v119, v229, v121
	v_mul_f32_e32 v119, 0x3fb8aa3b, v119
	v_add_f32_e32 v227, 0, v231
	v_exp_f32_e32 v119, v119
	v_add_f32_e32 v227, v227, v235
	v_add_f32_e32 v126, v227, v126
	v_cndmask_b32_e64 v118, v118, 0, s[78:79]
	v_add_f32_e32 v228, 0, v232
	v_add_f32_e32 v124, v126, v118
	v_cvt_pk_bf16_f32 v118, v118, s0
	v_add_f32_e32 v228, v228, v236
	ds_write_b16 v224, v118 offset:384
	v_mul_f32_e32 v118, v125, v119
	v_add_f32_e32 v127, v228, v127
	v_cndmask_b32_e64 v118, v118, 0, s[80:81]
	v_add_f32_e32 v125, v127, v118
	v_cvt_pk_bf16_f32 v118, v118, s0
	s_waitcnt vmcnt(8)
	v_mfma_f32_16x16x32_bf16 v[14:17], v[82:85], v[14:17], 0
	ds_write_b16 v224, v118 offset:528
	v_and_b32_e32 v118, 64, v128
	v_add_u32_e32 v127, 64, v118
	v_mfma_f32_16x16x32_bf16 v[118:121], v[82:85], v[62:65], 0
	v_xor_b32_e32 v126, 1, v128
	v_cmp_lt_i32_e32 vcc, v126, v127
	v_xor_b32_e32 v63, 2, v128
	v_mfma_f32_16x16x32_bf16 v[14:17], v[78:81], v[10:13], v[14:17]
	v_and_b32_e32 v11, 0xffff0000, v82
	v_lshlrev_b32_e32 v10, 16, v82
	s_waitcnt vmcnt(0)
	v_mul_f32_e32 v11, v115, v11
	v_cndmask_b32_e32 v62, v128, v126, vcc
	v_mfma_f32_16x16x32_bf16 v[58:61], v[78:81], v[58:61], v[118:121]
	v_fmac_f32_e32 v11, v114, v10
	v_lshlrev_b32_e32 v10, 16, v83
	v_lshlrev_b32_e32 v62, 2, v62
	v_fmac_f32_e32 v11, v116, v10
	v_and_b32_e32 v10, 0xffff0000, v83
	ds_bpermute_b32 v64, v62, v122
	v_fmac_f32_e32 v11, v117, v10
	v_lshlrev_b32_e32 v10, 16, v84
	v_fmac_f32_e32 v11, v110, v10
	v_and_b32_e32 v10, 0xffff0000, v84
	v_mfma_f32_16x16x32_bf16 v[54:57], v[74:77], v[54:57], v[58:61]
	v_fmac_f32_e32 v11, v111, v10
	v_lshlrev_b32_e32 v10, 16, v85
	v_cmp_lt_i32_e32 vcc, v63, v127
	v_fmac_f32_e32 v11, v112, v10
	v_and_b32_e32 v10, 0xffff0000, v85
	v_cndmask_b32_e32 v63, v128, v63, vcc
	v_fmac_f32_e32 v11, v113, v10
	v_and_b32_e32 v12, 0xffff0000, v78
	v_lshlrev_b32_e32 v60, 2, v63
	s_waitcnt lgkmcnt(0)
	v_add_f32_e32 v61, v122, v64
	v_mfma_f32_16x16x32_bf16 v[46:49], v[82:85], v[46:49], 0
	v_add_f32_e32 v10, 0, v11
	v_lshlrev_b32_e32 v11, 16, v78
	v_mul_f32_e32 v12, v107, v12
	v_mfma_f32_16x16x32_bf16 v[54:57], v[70:73], v[50:53], v[54:57]
	ds_bpermute_b32 v50, v60, v61
	v_fmac_f32_e32 v12, v106, v11
	v_lshlrev_b32_e32 v11, 16, v79
	v_fmac_f32_e32 v12, v108, v11
	v_and_b32_e32 v11, 0xffff0000, v79
	v_xor_b32_e32 v58, 4, v128
	v_fmac_f32_e32 v12, v109, v11
	v_lshlrev_b32_e32 v11, 16, v80
	v_cmp_lt_i32_e32 vcc, v58, v127
	v_mfma_f32_16x16x32_bf16 v[42:45], v[78:81], v[42:45], v[46:49]
	v_fmac_f32_e32 v12, v102, v11
	v_and_b32_e32 v11, 0xffff0000, v80
	v_cndmask_b32_e32 v51, v128, v58, vcc
	v_fmac_f32_e32 v12, v103, v11
	v_lshlrev_b32_e32 v11, 16, v81
	v_lshlrev_b32_e32 v59, 2, v51
	s_waitcnt lgkmcnt(0)
	v_add_f32_e32 v50, v61, v50
	v_fmac_f32_e32 v12, v104, v11
	v_and_b32_e32 v11, 0xffff0000, v81
	ds_bpermute_b32 v46, v59, v50
	v_fmac_f32_e32 v12, v105, v11
	v_mfma_f32_16x16x32_bf16 v[40:43], v[74:77], v[38:41], v[42:45]
	v_add_f32_e32 v10, v10, v12
	v_and_b32_e32 v12, 0xffff0000, v74
	v_lshlrev_b32_e32 v11, 16, v74
	v_mul_f32_e32 v12, v99, v12
	v_xor_b32_e32 v51, 8, v128
	v_fmac_f32_e32 v12, v98, v11
	v_lshlrev_b32_e32 v11, 16, v75
	v_cmp_lt_i32_e32 vcc, v51, v127
	v_fmac_f32_e32 v12, v100, v11
	v_and_b32_e32 v11, 0xffff0000, v75
	v_cndmask_b32_e32 v47, v128, v51, vcc
	s_waitcnt lgkmcnt(0)
	v_add_f32_e32 v38, v50, v46
	v_mfma_f32_16x16x32_bf16 v[50:53], v[70:73], v[34:37], v[40:43]
	v_fmac_f32_e32 v12, v101, v11
	v_lshlrev_b32_e32 v11, 16, v76
	ds_bpermute_b32 v36, v62, v124
	v_mfma_f32_16x16x32_bf16 v[32:35], v[82:85], v[30:33], 0
	v_fmac_f32_e32 v12, v94, v11
	v_and_b32_e32 v11, 0xffff0000, v76
	v_fmac_f32_e32 v12, v95, v11
	v_lshlrev_b32_e32 v11, 16, v77
	v_fmac_f32_e32 v12, v96, v11
	v_and_b32_e32 v11, 0xffff0000, v77
	v_mfma_f32_16x16x32_bf16 v[26:29], v[78:81], v[26:29], v[32:35]
	v_fmac_f32_e32 v12, v97, v11
	v_add_f32_e32 v10, v10, v12
	v_and_b32_e32 v12, 0xffff0000, v70
	ds_bpermute_b32 v39, v62, v123
	s_waitcnt lgkmcnt(1)
	v_add_f32_e32 v31, v124, v36
	ds_bpermute_b32 v33, v62, v125
	v_lshlrev_b32_e32 v11, 16, v70
	v_mul_f32_e32 v12, v91, v12
	ds_bpermute_b32 v36, v60, v31
	v_fmac_f32_e32 v12, v90, v11
	v_lshlrev_b32_e32 v11, 16, v71
	v_mfma_f32_16x16x32_bf16 v[22:25], v[74:77], v[22:25], v[26:29]
	v_fmac_f32_e32 v12, v92, v11
	v_and_b32_e32 v11, 0xffff0000, v71
	v_fmac_f32_e32 v12, v93, v11
	v_lshlrev_b32_e32 v11, 16, v72
	v_fmac_f32_e32 v12, v86, v11
	v_and_b32_e32 v11, 0xffff0000, v72
	s_waitcnt lgkmcnt(2)
	v_add_f32_e32 v37, v123, v39
	s_waitcnt lgkmcnt(1)
	v_add_f32_e32 v28, v125, v33
	v_fmac_f32_e32 v12, v87, v11
	v_lshlrev_b32_e32 v11, 16, v73
	ds_bpermute_b32 v39, v60, v37
	s_waitcnt lgkmcnt(1)
	v_add_f32_e32 v26, v31, v36
	v_mfma_f32_16x16x32_bf16 v[18:21], v[70:73], v[18:21], v[22:25]
	v_fmac_f32_e32 v12, v88, v11
	v_and_b32_e32 v11, 0xffff0000, v73
	ds_bpermute_b32 v27, v59, v26
	ds_bpermute_b32 v25, v60, v28
	v_fmac_f32_e32 v12, v89, v11
	v_add_f32_e32 v13, v10, v12
	v_xor_b32_e32 v10, 16, v128
	v_cmp_lt_i32_e32 vcc, v10, v127
	s_waitcnt lgkmcnt(2)
	v_add_f32_e32 v32, v37, v39
	s_waitcnt lgkmcnt(0)
	v_add_f32_e32 v25, v28, v25
	v_cndmask_b32_e32 v10, v128, v10, vcc
	v_lshlrev_b32_e32 v10, 2, v10
	ds_bpermute_b32 v34, v59, v32
	v_add_f32_e32 v24, v26, v27
	ds_bpermute_b32 v26, v59, v25
	ds_bpermute_b32 v27, v10, v13
	v_mfma_f32_16x16x32_bf16 v[14:17], v[74:77], v[6:9], v[14:17]
	v_xor_b32_e32 v7, 32, v128
	v_cmp_lt_i32_e32 vcc, v7, v127
	v_lshlrev_b32_e32 v58, 2, v47
	s_waitcnt lgkmcnt(2)
	v_add_f32_e32 v22, v32, v34
	v_cndmask_b32_e32 v7, v128, v7, vcc
	s_waitcnt lgkmcnt(1)
	v_add_f32_e32 v11, v25, v26
	s_waitcnt lgkmcnt(0)
	v_add_f32_e32 v6, v13, v27
	v_lshlrev_b32_e32 v7, 2, v7
	ds_bpermute_b32 v30, v58, v38
	ds_bpermute_b32 v23, v58, v22
	ds_bpermute_b32 v10, v58, v24
	ds_bpermute_b32 v12, v58, v11
	ds_bpermute_b32 v7, v7, v6
	v_mfma_f32_16x16x32_bf16 v[14:17], v[70:73], v[2:5], v[14:17]
	s_and_saveexec_b64 s[0:1], s[2:3]
	s_cbranch_execz .LBB0_625
	s_waitcnt lgkmcnt(0)
	v_add_f32_e32 v2, v6, v7
	ds_write_b32 v218, v2

; #define PG8_SETA(d0, d1, u) do { d0.x = PG8_OFFA(u, Rr[0], 0); d0.y = PG8_OFFA(u, Rr[1], 1); d1.x = PG8_OFFA(u, HALF + Rr[0], 0); d1.y = PG8_OFFA(u, HALF + Rr[1], 1); } while (0)
; template <class Epi, class Sched, bool GATHER, bool ALIGN_EPI, bool SP2, bool FP8>
; __device__ __forceinline__ void gemm_phase(LAS unsigned char* lds, const Gemm g, const Sched& S, const Epi& E) {
;     ...
;         const bool has_next = S.next(ui + 1, nxt);
;         const int nA = has_next ? (GATHER ? 0 : nxt.pm * tstep) : cA, nB = has_next ? nxt.pn * tstep : cB;
;         u32x2 nvA0 = vA0, nvA1 = vA1;
;         if constexpr (GATHER) { if (has_next) PG8_SETA(nvA0, nvA1, nxt); }
.LBB0_928:
	s_nop 0
	v_cndmask_b32_e64 v2, 0, 1, s[2:3]
	v_cmp_ne_u32_e64 s[0:1], 1, v2
	s_andn2_b64 vcc, exec, s[2:3]
	v_mov_b32_e32 v179, 0
	v_mov_b32_e32 v180, 0
	v_mov_b32_e32 v181, 0
	v_mov_b32_e32 v182, 0
	s_cbranch_vccnz .LBB0_930
	s_lshl_b32 s4, s74, 2
	s_add_i32 s4, s4, 0
	s_add_i32 s4, s4, 0x27e00
	v_mov_b32_e32 v2, s4
	ds_read_b32 v8, v2
	v_add_u32_e32 v2, s77, v1
	v_add_u32_e32 v4, s77, v171
	s_add_i32 s8, s77, 0x80
	v_add_u32_e32 v6, s8, v1
	s_waitcnt lgkmcnt(0)
	v_cmp_lt_i32_e32 vcc, v2, v8
	v_cmp_lt_i32_e64 s[4:5], v4, v8
	v_add_u32_e32 v9, s8, v171
	s_lshl_b32 s18, s74, 14
	v_cndmask_b32_e32 v2, 0, v2, vcc
	v_cndmask_b32_e64 v4, 0, v4, s[4:5]
	v_cmp_lt_i32_e64 s[6:7], v6, v8
	v_cmp_lt_i32_e64 s[8:9], v9, v8
	v_add_u32_e32 v2, s18, v2
	v_add_u32_e32 v4, s18, v4
	v_cndmask_b32_e64 v6, 0, v6, s[6:7]
	v_cndmask_b32_e64 v8, 0, v9, s[8:9]
	v_ashrrev_i32_e32 v3, 31, v2
	v_ashrrev_i32_e32 v5, 31, v4
	v_add_u32_e32 v6, s18, v6
	v_add_u32_e32 v8, s18, v8
	v_lshl_add_u64 v[2:3], v[2:3], 2, s[22:23]
	v_lshl_add_u64 v[4:5], v[4:5], 2, s[22:23]
	v_ashrrev_i32_e32 v7, 31, v6
	v_ashrrev_i32_e32 v9, 31, v8
	v_lshl_add_u64 v[6:7], v[6:7], 2, s[22:23]
	v_lshl_add_u64 v[8:9], v[8:9], 2, s[22:23]
	global_load_dword v179, v[2:3], off
	global_load_dword v180, v[4:5], off
	global_load_dword v181, v[6:7], off
	global_load_dword v182, v[8:9], off

; template <class Epi, class Sched, bool GATHER, bool ALIGN_EPI, bool SP2, bool FP8>
; __device__ __forceinline__ void gemm_phase(LAS unsigned char* lds, const Gemm g, const Sched& S, const Epi& E) {
;     ...
;             const bool last = (t == nt - 2);
;             if (last) pre = E.prefetch(cur, wr, wc, fr, fq);
;             const int a1 = cA + (t + 1) * kstep;
;             const int a2 = last ? nA : cA + (t + 2) * kstep, b2 = last ? nB : cB + (t + 2) * kstep;
;             const int a3 = a2 + kstep, b3 = b2 + kstep;
;             const u32x2 va20 = (GATHER && last) ? nvA0 : vA0, va21 = (GATHER && last) ? nvA1 : vA1;
;     __device__ __forceinline__ void operator()(const f32x4 (&acc)[2][2][4][2], const pg8::Unit& u, const Pre& pre, int wr, int wc, int fr, int fq) const {
;         const int e = u.e, cn = u.pn - e * 16, col = cn * 128 + wc * 32 + 8 * fq, ce = cnt[e];
;         const f32x4 g0 = pre.g0, g1 = pre.g1, u0 = pre.u0, u1 = pre.u1;
;         float rsv[8];
; #pragma unroll
;         for (int i = 0; i < 8; ++i) { const int p = u.r0 + (i >> 2) * 128 + wr * 64 + (i & 3) * 16 + fr; rsv[i] = list_rs[e * LIST_STRIDE + (p < ce ? p : 0)]; }
.LBB0_932:
	s_cmp_eq_u32 s5, 12
	s_cselect_b64 s[2:3], -1, 0
	s_cmp_lg_u32 s5, 12
	v_mov_b32_e32 v189, v186
	v_mov_b32_e32 v190, v184
	v_mov_b32_e32 v187, v183
	v_mov_b32_e32 v188, v185
	s_cbranch_scc1 .LBB0_931
	global_load_dwordx4 v[22:25], v[168:169], off offset:16
	global_load_dwordx4 v[26:29], v[168:169], off
	global_load_dwordx4 v[18:21], v[166:167], off offset:16
	global_load_dwordx4 v[30:33], v[166:167], off
	v_lshl_or_b32 v179, v179, 11, v172
	v_lshl_or_b32 v180, v180, 11, v172
	v_lshl_or_b32 v181, v181, 11, v172
	v_lshl_or_b32 v182, v182, 11, v172
	v_mov_b32_e32 v189, v182
	v_mov_b32_e32 v190, v181
	v_mov_b32_e32 v187, v179
	v_mov_b32_e32 v188, v180
	s_lshl_b32 s8, s33, 2
	s_add_i32 s8, s8, 0x27e00
	v_mov_b32_e32 v247, s8
	ds_read_b32 v247, v247
	v_readfirstlane_b32 s8, v0
	s_lshl_b32 s98, s33, 14
	s_nop 2
	s_ashr_i32 s8, s8, 2
	s_andn2_b32 s8, s8, 63
	v_and_or_b32 v246, v0, 15, s8
	v_add_u32_e32 v246, s50, v246
	v_add_u32_e32 v241, 16, v246
	v_add_u32_e32 v242, 32, v246
	v_add_u32_e32 v243, 48, v246
	s_waitcnt lgkmcnt(0)
	v_cmp_lt_i32_e32 vcc, v246, v247
	v_cmp_lt_i32_e64 s[100:101], v241, v247
	s_nop 1
	v_cndmask_b32_e32 v240, 0, v246, vcc
	v_cndmask_b32_e64 v241, 0, v241, s[100:101]
	v_cmp_lt_i32_e32 vcc, v242, v247
	v_cmp_lt_i32_e64 s[100:101], v243, v247
	v_add_lshl_u32 v240, v240, s98, 2
	v_add_lshl_u32 v241, v241, s98, 2
	v_cndmask_b32_e32 v242, 0, v242, vcc
	v_cndmask_b32_e64 v243, 0, v243, s[100:101]
	global_load_dword v240, v240, s[28:29]
	global_load_dword v241, v241, s[28:29]
	v_add_lshl_u32 v242, v242, s98, 2
	v_add_lshl_u32 v243, v243, s98, 2
	v_add_u32_e32 v246, 0x80, v246
	global_load_dword v242, v242, s[28:29]
	global_load_dword v243, v243, s[28:29]
	v_sub_u32_e32 v247, v247, v246
	s_nop 0
	v_cmp_lt_i32_e32 vcc, 0, v247
	v_cmp_lt_i32_e64 s[100:101], 16, v247
	v_add_u32_e32 v247, 16, v246
	s_nop 0
	v_cndmask_b32_e32 v246, 0, v246, vcc
	v_cndmask_b32_e64 v247, 0, v247, s[100:101]
	v_add_lshl_u32 v246, v246, s98, 2
	v_add_lshl_u32 v247, v247, s98, 2
	global_load_dword v246, v246, s[28:29]
	global_load_dword v247, v247, s[28:29]
	s_branch .LBB0_931
